# P4 attention key loop: window-edge mask un-if-converted (15 of 17 key tiles skip 32 index/compare VALU + 16 SALU, 16 selects become moves); on top of v74
# speedup vs baseline: 1.0136x; 1.0136x over previous
; #define LAS __attribute__((address_space(3)))
; DI int crow(int i, int h) { return (i & 3) + 8 * (i >> 2) + 4 * h; }
; #define MFMA32(a, b, c) __builtin_amdgcn_mfma_f32_32x32x16_bf16((a), (b), (c), 0, 0, 0)
; DI void attn_unit(LAS unsigned char* ldsb, const bf16* proj, const bf16* KR, const bf16* VTg, const float* rope, const float* sinks, unsigned char* yab, int kvh, int ab) {
;     ...
;             const bool lat = kt >= 8; const int j = kt - 8, T = Tq + j, kb = kb0 + 32 * j, slot = (T + 2 * NSLOT) % NSLOT;
;             if (lat && (T < 0 || T >= NTOK / 32)) continue;
;             const LAS unsigned char* Kb = lat ? KL + (32 * slot + r) * KRS : KC + (32 * kt + r) * KRS;
;             const LAS unsigned char* Vb = lat ? VL + r * VLRS + 64 * slot : VC + r * VCRS + 64 * kt;
;             const int vrs32 = 32 * (lat ? VLRS : VCRS); const bool edge = lat && (j == 0 || j == 8);
;             f32x16 s;
; #pragma unroll
;             for (int i = 0; i < 16; ++i) s[i] = 0.f;
; #pragma unroll
;             for (int ks = 0; ks < 4; ++ks) { const bf16x8 kf = *(const LAS bf16x8*)(Kb + (16 * ks + 8 * h5) * 2); s = MFMA32(kf, qf[ks], s); }
;             float mt = -INFINITY;
; #pragma unroll
;             for (int i = 0; i < 16; ++i) { float v = s[i];
;                 if (edge) { const int dk = kb + crow(i, h5) - qp; if (dk > 128 || dk < -128) v = -INFINITY; }
;                 s[i] = v; mt = fmaxf(mt, v); }
;             mt = fmaxf(mt, __shfl_xor(mt, 32));
;             if (__any(mt > m_run + 8.0f)) { const float mn = fmaxf(m_run, mt); const float alpha = __builtin_amdgcn_exp2f(m_run - mn); l_run *= alpha; m_run = mn;
; #pragma unroll
;                 for (int i = 0; i < 16; ++i) { o0[i] *= alpha; o1[i] *= alpha; } }
.LBB0_1312:
	s_cmp_gt_u32 s55, 7
	s_cselect_b64 s[4:5], -1, 0
	s_add_i32 s6, s65, s55
	s_add_i32 s6, s6, -12
	s_cmpk_gt_u32 s6, 0x1ff
	s_cselect_b64 s[6:7], -1, 0
	s_and_b64 s[6:7], s[4:5], s[6:7]
	s_and_b64 vcc, exec, s[6:7]
	s_cbranch_vccnz .LBB0_1311
	s_mul_hi_u32 s6, s54, 0xcccccccd
	s_lshr_b32 s71, s6, 3
	s_mul_i32 s6, s71, 10
	s_sub_i32 s6, s35, s6
	s_add_i32 s72, s55, -8
	s_add_i32 s8, s55, s6
	s_and_b64 s[6:7], s[4:5], exec
	s_cselect_b32 s6, s8, s55
	v_lshl_or_b32 v3, s6, 5, v1
	s_cselect_b32 s7, s3, 0
	v_mul_lo_u32 v3, v3, s45
	v_add3_u32 v3, s7, v3, v92
	ds_read_b128 v[36:39], v3
	ds_read_b128 v[180:183], v3 offset:32
	ds_read_b128 v[184:187], v3 offset:64
	s_waitcnt lgkmcnt(2)
	v_mfma_f32_32x32x16_bf16 v[36:51], v[36:39], v[72:75], 0
	s_and_b32 s72, s72, -9
	v_add_u32_e32 v188, s24, v169
	s_cmp_eq_u32 s72, 0
	v_add_u32_e32 v179, 0xfffffdff, v188
	s_cselect_b64 s[72:73], -1, 0
	v_add_u32_e32 v189, 0xfffffe00, v188
	v_cmp_gt_u32_e32 vcc, s59, v179
	s_waitcnt lgkmcnt(1)
	v_mfma_f32_32x32x16_bf16 v[36:51], v[180:183], v[80:83], v[36:51]
	ds_read_b128 v[180:183], v3 offset:96
	s_and_b64 s[72:73], s[4:5], s[72:73]
	s_cbranch_scc1 .Lp4_edge
	s_waitcnt lgkmcnt(1)
	v_mfma_f32_32x32x16_bf16 v[36:51], v[184:187], v[76:79], v[36:51]
	s_waitcnt lgkmcnt(0)
	v_mfma_f32_32x32x16_bf16 v[36:51], v[180:183], v[84:87], v[36:51]
	s_nop 11
	v_mov_b32_e32 v183, v36
	v_mov_b32_e32 v182, v37
	v_mov_b32_e32 v181, v38
	v_mov_b32_e32 v180, v39
	v_mov_b32_e32 v179, v40
	v_mov_b32_e32 v40, v41
	v_mov_b32_e32 v41, v42
	v_mov_b32_e32 v42, v43
	v_max3_f32 v3, v183, s61, v182
	v_mov_b32_e32 v43, v45
	v_max3_f32 v3, v3, v181, v180
	v_max3_f32 v3, v3, v179, v40
	v_mov_b32_e32 v45, v46
	v_max3_f32 v3, v3, v41, v42
	v_max3_f32 v3, v3, v44, v43
	v_mov_b32_e32 v39, v47
	v_max3_f32 v37, v3, v45, v39
	v_mov_b32_e32 v3, v48
	s_nop 0
	v_mov_b32_e32 v36, v49
	v_max3_f32 v46, v37, v3, v36
	v_mov_b32_e32 v38, v50
	s_nop 0
	v_mov_b32_e32 v37, v51
	v_max3_f32 v46, v46, v38, v37
	s_branch .Lp4_join
.Lp4_edge:
	v_add_u32_e32 v190, 0xfffffe01, v188
	v_cmp_gt_u32_e64 s[6:7], s59, v189
	s_and_b64 vcc, s[72:73], vcc
	v_add_u32_e32 v191, 0xfffffe02, v188
	v_cmp_gt_u32_e64 s[8:9], s59, v190
	s_waitcnt lgkmcnt(1)
	v_mfma_f32_32x32x16_bf16 v[36:51], v[184:187], v[76:79], v[36:51]
	v_add_u32_e32 v192, 0xfffffe07, v188
	v_cmp_gt_u32_e64 s[10:11], s59, v191
	v_add_u32_e32 v193, 0xfffffe08, v188
	v_cmp_gt_u32_e64 s[12:13], s59, v192
	v_add_u32_e32 v194, 0xfffffe09, v188
	v_cmp_gt_u32_e64 s[14:15], s59, v193
	v_cmp_gt_u32_e64 s[16:17], s59, v194
	s_waitcnt lgkmcnt(0)
	v_mfma_f32_32x32x16_bf16 v[36:51], v[180:183], v[84:87], v[36:51]
	s_nop 11
	v_cndmask_b32_e32 v183, v36, v172, vcc
	s_and_b64 vcc, s[72:73], s[6:7]
	v_cndmask_b32_e32 v182, v37, v172, vcc
	s_and_b64 vcc, s[72:73], s[8:9]
	v_cndmask_b32_e32 v181, v38, v172, vcc
	s_and_b64 vcc, s[72:73], s[10:11]
	v_cndmask_b32_e32 v180, v39, v172, vcc
	s_and_b64 vcc, s[72:73], s[12:13]
	v_cndmask_b32_e32 v179, v40, v172, vcc
	s_and_b64 vcc, s[72:73], s[14:15]
	v_cndmask_b32_e32 v40, v41, v172, vcc
	s_and_b64 vcc, s[72:73], s[16:17]
	v_add_u32_e32 v36, 0xfffffe0a, v188
	v_cndmask_b32_e32 v41, v42, v172, vcc
	v_cmp_gt_u32_e32 vcc, s59, v36
	s_and_b64 vcc, s[72:73], vcc
	v_add_u32_e32 v36, 0xfffffe0f, v188
	v_cndmask_b32_e32 v42, v43, v172, vcc
	v_cmp_gt_u32_e32 vcc, s59, v36
	s_and_b64 vcc, s[72:73], vcc
	v_add_u32_e32 v36, 0xfffffe10, v188
	v_cndmask_b32_e32 v44, v44, v172, vcc
	v_cmp_gt_u32_e32 vcc, s59, v36
	s_and_b64 vcc, s[72:73], vcc
	v_add_u32_e32 v36, 0xfffffe11, v188
	v_max3_f32 v3, v183, s61, v182
	v_cndmask_b32_e32 v43, v45, v172, vcc
	v_cmp_gt_u32_e32 vcc, s59, v36
	v_max3_f32 v3, v3, v181, v180
	s_and_b64 vcc, s[72:73], vcc
	v_add_u32_e32 v36, 0xfffffe12, v188
	v_max3_f32 v3, v3, v179, v40
	v_cndmask_b32_e32 v45, v46, v172, vcc
	v_cmp_gt_u32_e32 vcc, s59, v36
	v_max3_f32 v3, v3, v41, v42
	s_and_b64 vcc, s[72:73], vcc
	v_max3_f32 v3, v3, v44, v43
	v_cndmask_b32_e32 v39, v47, v172, vcc
	v_max3_f32 v37, v3, v45, v39
	v_add_u32_e32 v3, 0xfffffe17, v188
	v_cmp_gt_u32_e32 vcc, s59, v3
	s_and_b64 vcc, s[72:73], vcc
	v_add_u32_e32 v36, 0xfffffe18, v188
	v_cndmask_b32_e32 v3, v48, v172, vcc
	v_cmp_gt_u32_e32 vcc, s59, v36
	s_and_b64 vcc, s[72:73], vcc
	s_nop 0
	v_cndmask_b32_e32 v36, v49, v172, vcc
	v_max3_f32 v46, v37, v3, v36
	v_add_u32_e32 v37, 0xfffffe19, v188
	v_cmp_gt_u32_e32 vcc, s59, v37
	s_and_b64 vcc, s[72:73], vcc
	v_add_u32_e32 v37, 0xfffffe1a, v188
	v_cndmask_b32_e32 v38, v50, v172, vcc
	v_cmp_gt_u32_e32 vcc, s59, v37
	s_and_b64 vcc, s[72:73], vcc
	s_nop 0
	v_cndmask_b32_e32 v37, v51, v172, vcc
	v_max3_f32 v46, v46, v38, v37
.Lp4_join:
	v_mov_b32_e32 v47, v46
	s_waitcnt lgkmcnt(0)
	s_nop 0
	v_permlane32_swap_b32 v46, v47
	v_max_f32_e32 v46, v46, v47
	v_add_f32_e32 v47, 0x41000000, v178
	v_cmp_gt_f32_e32 vcc, v46, v47
	s_cbranch_vccz .LBB0_1310
	v_max_f32_e32 v46, v46, v46
	v_max_f32_e32 v47, v178, v178
	v_max_f32_e32 v47, v47, v46
	v_sub_f32_e32 v46, v178, v47
	v_exp_f32_e32 v46, v46
	v_mov_b32_e32 v178, v47
	v_pk_mul_f32 v[34:35], v[34:35], v[46:47] op_sel_hi:[1,0]
	v_pk_mul_f32 v[32:33], v[32:33], v[46:47] op_sel_hi:[1,0]
	v_pk_mul_f32 v[30:31], v[30:31], v[46:47] op_sel_hi:[1,0]
	v_pk_mul_f32 v[28:29], v[28:29], v[46:47] op_sel_hi:[1,0]
	v_pk_mul_f32 v[26:27], v[26:27], v[46:47] op_sel_hi:[1,0]
	v_pk_mul_f32 v[24:25], v[24:25], v[46:47] op_sel_hi:[1,0]
	v_pk_mul_f32 v[22:23], v[22:23], v[46:47] op_sel_hi:[1,0]
	v_pk_mul_f32 v[20:21], v[20:21], v[46:47] op_sel_hi:[1,0]
	v_pk_mul_f32 v[18:19], v[18:19], v[46:47] op_sel_hi:[1,0]
	v_pk_mul_f32 v[16:17], v[16:17], v[46:47] op_sel_hi:[1,0]
	v_pk_mul_f32 v[14:15], v[14:15], v[46:47] op_sel_hi:[1,0]
	v_pk_mul_f32 v[12:13], v[12:13], v[46:47] op_sel_hi:[1,0]
	v_pk_mul_f32 v[10:11], v[10:11], v[46:47] op_sel_hi:[1,0]
	v_pk_mul_f32 v[8:9], v[8:9], v[46:47] op_sel_hi:[1,0]
	v_pk_mul_f32 v[6:7], v[6:7], v[46:47] op_sel_hi:[1,0]
	v_pk_mul_f32 v[4:5], v[4:5], v[46:47] op_sel_hi:[1,0]
	v_mul_f32_e32 v175, v175, v46
	s_branch .LBB0_1310
